# baseline (speedup 1.0000x reference)
.LBB0_6:
	s_andn2_b64 vcc, exec, s[0:1]
	s_cbranch_vccnz .LBB0_19
	s_cmpk_gt_u32 s2, 0x4c7
	s_mov_b64 s[0:1], -1
	s_cbranch_scc0 .LBB0_17
	s_cmpk_gt_u32 s2, 0x587
	s_cbranch_scc0 .LBB0_14
	v_lshrrev_b32_e32 v5, 6, v0
	v_and_b32_e32 v2, 63, v0
	v_mul_u32_u24_e32 v1, 0x104, v5
	s_cmpk_gt_u32 s2, 0x707
	v_mov_b32_e32 v3, 0
	v_lshl_add_u32 v1, v2, 2, v1
	v_or_b32_e32 v4, 4, v5
	v_lshlrev_b32_e32 v2, 2, v2
	s_cbranch_scc0 .LBB0_11
	s_add_i32 s0, s2, 0xf8f8
	s_and_b32 s1, s0, 0xffff
	s_mul_i32 s1, s1, 0xaaab
	s_lshr_b32 s1, s1, 20
	s_mul_i32 s3, s1, 24
	s_sub_i32 s0, s0, s3
	s_lshl_b32 s0, s0, 6
	s_and_b32 s0, s0, 0xffc0
	s_lshl_b32 s3, s1, 6
	s_waitcnt lgkmcnt(0)
	s_lshl_b32 s4, s0, 2
	s_add_u32 s4, s20, s4
	v_or_b32_e32 v24, s3, v5
	s_addc_u32 s5, s21, 0
	v_mul_u32_u24_e32 v8, 0x600, v24
	v_or_b32_e32 v10, s3, v4
	v_or_b32_e32 v12, 8, v24
	v_or_b32_e32 v14, 12, v24
	v_or_b32_e32 v16, 16, v24
	v_or_b32_e32 v18, 20, v24
	v_or_b32_e32 v20, 24, v24
	v_or_b32_e32 v22, 28, v24
	v_lshl_add_u64 v[6:7], s[4:5], 0, v[2:3]
	v_lshlrev_b32_e32 v8, 2, v8
	v_mov_b32_e32 v9, v3
	v_mul_u32_u24_e32 v10, 0x600, v10
	v_mul_u32_u24_e32 v12, 0x600, v12
	v_mul_u32_u24_e32 v14, 0x600, v14
	v_mul_u32_u24_e32 v16, 0x600, v16
	v_mul_u32_u24_e32 v18, 0x600, v18
	v_mul_u32_u24_e32 v20, 0x600, v20
	v_mul_u32_u24_e32 v22, 0x600, v22
	v_lshl_add_u64 v[8:9], v[6:7], 0, v[8:9]
	v_lshlrev_b32_e32 v10, 2, v10
	v_mov_b32_e32 v11, v3
	v_lshlrev_b32_e32 v12, 2, v12
	v_mov_b32_e32 v13, v3
	v_lshlrev_b32_e32 v14, 2, v14
	v_mov_b32_e32 v15, v3
	v_lshlrev_b32_e32 v16, 2, v16
	v_mov_b32_e32 v17, v3
	v_lshlrev_b32_e32 v18, 2, v18
	v_mov_b32_e32 v19, v3
	v_lshlrev_b32_e32 v20, 2, v20
	v_mov_b32_e32 v21, v3
	v_lshlrev_b32_e32 v22, 2, v22
	v_mov_b32_e32 v23, v3
	v_lshl_add_u64 v[10:11], v[6:7], 0, v[10:11]
	v_lshl_add_u64 v[12:13], v[6:7], 0, v[12:13]
	v_lshl_add_u64 v[14:15], v[6:7], 0, v[14:15]
	v_lshl_add_u64 v[16:17], v[6:7], 0, v[16:17]
	v_lshl_add_u64 v[18:19], v[6:7], 0, v[18:19]
	v_lshl_add_u64 v[20:21], v[6:7], 0, v[20:21]
	v_lshl_add_u64 v[22:23], v[6:7], 0, v[22:23]
	global_load_dword v25, v[8:9], off nt
	global_load_dword v26, v[10:11], off nt
	global_load_dword v27, v[12:13], off nt
	global_load_dword v28, v[14:15], off nt
	global_load_dword v29, v[16:17], off nt
	global_load_dword v30, v[18:19], off nt
	global_load_dword v31, v[20:21], off nt
	global_load_dword v32, v[22:23], off nt
	v_or_b32_e32 v8, 32, v24
	v_mul_u32_u24_e32 v8, 0x600, v8
	v_or_b32_e32 v10, 36, v24
	v_or_b32_e32 v12, 40, v24
	v_or_b32_e32 v14, 44, v24
	v_or_b32_e32 v16, 48, v24
	v_or_b32_e32 v18, 52, v24
	v_or_b32_e32 v20, 56, v24
	v_or_b32_e32 v22, 60, v24
	v_lshlrev_b32_e32 v8, 2, v8
	v_mov_b32_e32 v9, v3
	v_mul_u32_u24_e32 v10, 0x600, v10
	v_mul_u32_u24_e32 v12, 0x600, v12
	v_mul_u32_u24_e32 v14, 0x600, v14
	v_mul_u32_u24_e32 v16, 0x600, v16
	v_mul_u32_u24_e32 v18, 0x600, v18
	v_mul_u32_u24_e32 v20, 0x600, v20
	v_mul_u32_u24_e32 v22, 0x600, v22
	v_lshl_add_u64 v[8:9], v[6:7], 0, v[8:9]
	v_lshlrev_b32_e32 v10, 2, v10
	v_mov_b32_e32 v11, v3
	v_lshlrev_b32_e32 v12, 2, v12
	v_mov_b32_e32 v13, v3
	v_lshlrev_b32_e32 v14, 2, v14
	v_mov_b32_e32 v15, v3
	v_lshlrev_b32_e32 v16, 2, v16
	v_mov_b32_e32 v17, v3
	v_lshlrev_b32_e32 v18, 2, v18
	v_mov_b32_e32 v19, v3
	v_lshlrev_b32_e32 v20, 2, v20
	v_mov_b32_e32 v21, v3
	v_lshlrev_b32_e32 v22, 2, v22
	v_mov_b32_e32 v23, v3
	v_lshl_add_u64 v[10:11], v[6:7], 0, v[10:11]
	v_lshl_add_u64 v[12:13], v[6:7], 0, v[12:13]
	v_lshl_add_u64 v[14:15], v[6:7], 0, v[14:15]
	v_lshl_add_u64 v[16:17], v[6:7], 0, v[16:17]
	v_lshl_add_u64 v[18:19], v[6:7], 0, v[18:19]
	v_lshl_add_u64 v[20:21], v[6:7], 0, v[20:21]
	v_lshl_add_u64 v[6:7], v[6:7], 0, v[22:23]
	global_load_dword v22, v[8:9], off nt
	global_load_dword v23, v[10:11], off nt
	global_load_dword v24, v[12:13], off nt
	global_load_dword v33, v[14:15], off nt
	global_load_dword v34, v[16:17], off nt
	global_load_dword v35, v[18:19], off nt
	global_load_dword v36, v[20:21], off nt
	global_load_dword v37, v[6:7], off nt
	v_lshlrev_b32_e32 v6, 3, v0
	v_and_b32_e32 v8, 56, v6
	s_waitcnt vmcnt(15)
	ds_write_b32 v1, v25
	s_waitcnt vmcnt(14)
	ds_write_b32 v1, v26 offset:1040
	s_waitcnt vmcnt(13)
	ds_write_b32 v1, v27 offset:2080
	s_waitcnt vmcnt(12)
	ds_write_b32 v1, v28 offset:3120
	s_waitcnt vmcnt(11)
	ds_write_b32 v1, v29 offset:4160
	s_waitcnt vmcnt(10)
	ds_write_b32 v1, v30 offset:5200
	s_waitcnt vmcnt(9)
	ds_write_b32 v1, v31 offset:6240
	s_waitcnt vmcnt(8)
	ds_write_b32 v1, v32 offset:7280
	s_waitcnt vmcnt(7)
	ds_write_b32 v1, v22 offset:8320
	s_waitcnt vmcnt(6)
	ds_write_b32 v1, v23 offset:9360
	s_waitcnt vmcnt(5)
	ds_write_b32 v1, v24 offset:10400
	s_waitcnt vmcnt(4)
	ds_write_b32 v1, v33 offset:11440
	s_waitcnt vmcnt(3)
	ds_write_b32 v1, v34 offset:12480
	s_waitcnt vmcnt(2)
	ds_write_b32 v1, v35 offset:13520
	s_waitcnt vmcnt(1)
	ds_write_b32 v1, v36 offset:14560
	s_waitcnt vmcnt(0)
	ds_write_b32 v1, v37 offset:15600
	v_lshrrev_b32_e32 v28, 3, v0
	v_lshlrev_b32_e32 v6, 1, v8
	v_mul_u32_u24_e32 v8, 0x104, v8
	v_lshl_add_u32 v8, v28, 2, v8
	v_add_u32_e32 v9, 0x400, v8
	s_waitcnt lgkmcnt(0)
	s_barrier
	ds_read2_b32 v[10:11], v8 offset1:32
	ds_read2_b32 v[12:13], v8 offset0:130 offset1:162
	ds_read2_b32 v[14:15], v9 offset0:4 offset1:36
	ds_read2_b32 v[16:17], v9 offset0:134 offset1:166
	ds_read2_b32 v[18:19], v9 offset0:199 offset1:231
	ds_read2_b32 v[20:21], v9 offset0:69 offset1:101
	ds_read2_b32 v[22:23], v8 offset0:195 offset1:227
	ds_read2_b32 v[24:25], v8 offset0:65 offset1:97
	s_lshl_b32 s1, s1, 7
	s_add_u32 s4, s10, s1
	s_addc_u32 s5, s11, 0
	v_mov_b32_e32 v7, v3
	v_lshl_add_u64 v[6:7], s[4:5], 0, v[6:7]
	s_mov_b64 s[4:5], 0x600000
	v_lshl_add_u64 v[26:27], v[6:7], 0, s[4:5]
	s_waitcnt lgkmcnt(0)
	v_cvt_pk_f16_f32 v6, v10, v24
	v_or_b32_e32 v10, s0, v28
	v_lshlrev_b32_e32 v28, 11, v10
	v_mov_b32_e32 v29, v3
	v_cvt_pk_f16_f32 v9, v16, v18
	v_cvt_pk_f16_f32 v8, v14, v20
	v_cvt_pk_f16_f32 v7, v12, v22
	v_lshl_add_u64 v[30:31], v[26:27], 0, v[28:29]
	global_store_dwordx4 v[30:31], v[6:9], off sc1
	v_or_b32_e32 v10, 0x10000, v28
	s_mov_b64 s[0:1], 0
	v_cvt_pk_f16_f32 v6, v11, v25
	v_mov_b32_e32 v11, v3
	v_cvt_pk_f16_f32 v9, v17, v19
	v_cvt_pk_f16_f32 v8, v15, v21
	v_cvt_pk_f16_f32 v7, v13, v23
	v_lshl_add_u64 v[10:11], v[26:27], 0, v[10:11]
	global_store_dwordx4 v[10:11], v[6:9], off sc1
.LBB0_11:
	s_andn2_b64 vcc, exec, s[0:1]
	s_cbranch_vccnz .LBB0_13
	s_add_i32 s0, s2, 0xfa78
	s_and_b32 s1, s0, 0xffff
	s_mul_i32 s1, s1, 0xaaab
	s_lshr_b32 s1, s1, 20
	s_mul_i32 s3, s1, 24
	s_sub_i32 s0, s0, s3
	s_lshl_b32 s0, s0, 6
	s_and_b32 s0, s0, 0xffc0
	s_lshl_b32 s3, s1, 6
	s_waitcnt lgkmcnt(0)
	s_lshl_b32 s4, s0, 2
	s_add_u32 s4, s18, s4
	s_addc_u32 s5, s19, 0
	v_mov_b32_e32 v3, 0
	v_or_b32_e32 v22, s3, v5
	v_lshl_add_u64 v[6:7], s[4:5], 0, v[2:3]
	v_mul_u32_u24_e32 v2, 0x600, v22
	v_lshlrev_b32_e32 v2, 2, v2
	v_lshl_add_u64 v[8:9], v[6:7], 0, v[2:3]
	v_or_b32_e32 v2, s3, v4
	v_mul_u32_u24_e32 v2, 0x600, v2
	v_lshlrev_b32_e32 v2, 2, v2
	v_lshl_add_u64 v[4:5], v[6:7], 0, v[2:3]
	v_or_b32_e32 v2, 8, v22
	v_mul_u32_u24_e32 v2, 0x600, v2
	v_lshlrev_b32_e32 v2, 2, v2
	v_lshl_add_u64 v[10:11], v[6:7], 0, v[2:3]
	v_or_b32_e32 v2, 12, v22
	v_mul_u32_u24_e32 v2, 0x600, v2
	v_lshlrev_b32_e32 v2, 2, v2
	v_lshl_add_u64 v[12:13], v[6:7], 0, v[2:3]
	v_or_b32_e32 v2, 16, v22
	v_mul_u32_u24_e32 v2, 0x600, v2
	v_lshlrev_b32_e32 v2, 2, v2
	v_lshl_add_u64 v[14:15], v[6:7], 0, v[2:3]
	v_or_b32_e32 v2, 20, v22
	v_mul_u32_u24_e32 v2, 0x600, v2
	v_lshlrev_b32_e32 v2, 2, v2
	v_lshl_add_u64 v[16:17], v[6:7], 0, v[2:3]
	v_or_b32_e32 v2, 24, v22
	v_mul_u32_u24_e32 v2, 0x600, v2
	v_lshlrev_b32_e32 v2, 2, v2
	v_lshl_add_u64 v[18:19], v[6:7], 0, v[2:3]
	v_or_b32_e32 v2, 28, v22
	v_mul_u32_u24_e32 v2, 0x600, v2
	v_lshlrev_b32_e32 v2, 2, v2
	v_lshl_add_u64 v[20:21], v[6:7], 0, v[2:3]
	v_or_b32_e32 v2, 32, v22
	v_mul_u32_u24_e32 v2, 0x600, v2
	v_lshlrev_b32_e32 v2, 2, v2
	global_load_dword v23, v[8:9], off nt
	global_load_dword v24, v[4:5], off nt
	global_load_dword v25, v[10:11], off nt
	global_load_dword v26, v[12:13], off nt
	global_load_dword v27, v[14:15], off nt
	global_load_dword v28, v[16:17], off nt
	global_load_dword v29, v[18:19], off nt
	global_load_dword v30, v[20:21], off nt
	v_lshl_add_u64 v[4:5], v[6:7], 0, v[2:3]
	v_or_b32_e32 v2, 36, v22
	v_mul_u32_u24_e32 v2, 0x600, v2
	v_lshlrev_b32_e32 v2, 2, v2
	v_lshl_add_u64 v[8:9], v[6:7], 0, v[2:3]
	v_or_b32_e32 v2, 40, v22
	v_mul_u32_u24_e32 v2, 0x600, v2
	v_lshlrev_b32_e32 v2, 2, v2
	v_lshl_add_u64 v[10:11], v[6:7], 0, v[2:3]
	v_or_b32_e32 v2, 44, v22
	v_mul_u32_u24_e32 v2, 0x600, v2
	v_lshlrev_b32_e32 v2, 2, v2
	v_lshl_add_u64 v[12:13], v[6:7], 0, v[2:3]
	v_or_b32_e32 v2, 48, v22
	v_mul_u32_u24_e32 v2, 0x600, v2
	v_lshlrev_b32_e32 v2, 2, v2
	v_lshl_add_u64 v[14:15], v[6:7], 0, v[2:3]
	v_or_b32_e32 v2, 52, v22
	v_mul_u32_u24_e32 v2, 0x600, v2
	v_lshlrev_b32_e32 v2, 2, v2
	v_lshl_add_u64 v[16:17], v[6:7], 0, v[2:3]
	v_or_b32_e32 v2, 56, v22
	v_mul_u32_u24_e32 v2, 0x600, v2
	v_lshlrev_b32_e32 v2, 2, v2
	v_lshl_add_u64 v[18:19], v[6:7], 0, v[2:3]
	v_or_b32_e32 v2, 60, v22
	v_mul_u32_u24_e32 v2, 0x600, v2
	v_lshlrev_b32_e32 v2, 2, v2
	v_lshl_add_u64 v[6:7], v[6:7], 0, v[2:3]
	global_load_dword v2, v[4:5], off nt
	global_load_dword v20, v[8:9], off nt
	global_load_dword v21, v[10:11], off nt
	global_load_dword v22, v[12:13], off nt
	global_load_dword v31, v[14:15], off nt
	global_load_dword v32, v[16:17], off nt
	global_load_dword v33, v[18:19], off nt
	global_load_dword v34, v[6:7], off nt
	s_lshl_b32 s1, s1, 7
	s_add_u32 s4, s10, s1
	s_addc_u32 s5, s11, 0
	s_waitcnt vmcnt(15)
	ds_write_b32 v1, v23
	s_waitcnt vmcnt(14)
	ds_write_b32 v1, v24 offset:1040
	s_waitcnt vmcnt(13)
	ds_write_b32 v1, v25 offset:2080
	s_waitcnt vmcnt(12)
	ds_write_b32 v1, v26 offset:3120
	s_waitcnt vmcnt(11)
	ds_write_b32 v1, v27 offset:4160
	s_waitcnt vmcnt(10)
	ds_write_b32 v1, v28 offset:5200
	s_waitcnt vmcnt(9)
	ds_write_b32 v1, v29 offset:6240
	s_waitcnt vmcnt(8)
	ds_write_b32 v1, v30 offset:7280
	s_waitcnt vmcnt(7)
	ds_write_b32 v1, v2 offset:8320
	s_waitcnt vmcnt(6)
	ds_write_b32 v1, v20 offset:9360
	s_waitcnt vmcnt(5)
	ds_write_b32 v1, v21 offset:10400
	s_waitcnt vmcnt(4)
	ds_write_b32 v1, v22 offset:11440
	s_waitcnt vmcnt(3)
	ds_write_b32 v1, v31 offset:12480
	s_waitcnt vmcnt(2)
	ds_write_b32 v1, v32 offset:13520
	s_waitcnt vmcnt(1)
	ds_write_b32 v1, v33 offset:14560
	s_waitcnt vmcnt(0)
	ds_write_b32 v1, v34 offset:15600
	v_lshlrev_b32_e32 v2, 3, v0
	v_and_b32_e32 v6, 56, v2
	v_lshlrev_b32_e32 v2, 1, v6
	v_lshrrev_b32_e32 v1, 3, v0
	v_lshl_add_u64 v[4:5], s[4:5], 0, v[2:3]
	v_mul_u32_u24_e32 v2, 0x104, v6
	v_lshl_add_u32 v2, v1, 2, v2
	v_add_u32_e32 v6, 0x400, v2
	s_waitcnt lgkmcnt(0)
	s_barrier
	ds_read2_b32 v[8:9], v2 offset1:32
	ds_read2_b32 v[10:11], v2 offset0:130 offset1:162
	ds_read2_b32 v[12:13], v6 offset0:4 offset1:36
	ds_read2_b32 v[14:15], v6 offset0:134 offset1:166
	ds_read2_b32 v[16:17], v6 offset0:199 offset1:231
	ds_read2_b32 v[18:19], v6 offset0:69 offset1:101
	ds_read2_b32 v[20:21], v2 offset0:195 offset1:227
	ds_read2_b32 v[22:23], v2 offset0:65 offset1:97
	s_mov_b64 s[4:5], 0x300000
	v_or_b32_e32 v1, s0, v1
	v_lshl_add_u64 v[24:25], v[4:5], 0, s[4:5]
	v_lshlrev_b32_e32 v2, 11, v1
	s_waitcnt lgkmcnt(3)
	v_cvt_pk_f16_f32 v7, v14, v16
	s_waitcnt lgkmcnt(2)
	v_cvt_pk_f16_f32 v6, v12, v18
	s_waitcnt lgkmcnt(1)
	v_cvt_pk_f16_f32 v5, v10, v20
	s_waitcnt lgkmcnt(0)
	v_cvt_pk_f16_f32 v4, v8, v22
	v_lshl_add_u64 v[26:27], v[24:25], 0, v[2:3]
	v_or_b32_e32 v2, 0x10000, v2
	global_store_dwordx4 v[26:27], v[4:7], off sc1
	v_lshl_add_u64 v[2:3], v[24:25], 0, v[2:3]
	s_nop 0
	v_cvt_pk_f16_f32 v7, v15, v17
	v_cvt_pk_f16_f32 v6, v13, v19
	v_cvt_pk_f16_f32 v5, v11, v21
	v_cvt_pk_f16_f32 v4, v9, v23
	global_store_dwordx4 v[2:3], v[4:7], off sc1

.LBB0_14:
	s_andn2_b64 vcc, exec, s[0:1]
	s_cbranch_vccnz .LBB0_16
	s_add_i32 s0, s2, 56
	s_and_b32 s1, s0, 0xff
	s_mulk_i32 s1, 0xab
	s_bfe_u32 s1, s1, 0x5000b
	s_mul_i32 s3, s1, 12
	s_sub_i32 s0, s0, s3
	s_and_b32 s0, s0, 0xff
	s_lshl_b32 s3, s0, 8
	v_and_b32_e32 v1, 63, v0
	v_lshrrev_b32_e32 v8, 6, v0
	s_waitcnt lgkmcnt(0)
	s_add_u32 s4, s16, s3
	s_addc_u32 s5, s17, 0
	v_lshlrev_b32_e32 v6, 2, v1
	v_mov_b32_e32 v7, 0
	v_lshl_or_b32 v1, s1, 6, v8
	s_movk_i32 s3, 0x104
	v_lshl_add_u64 v[2:3], s[4:5], 0, v[6:7]
	v_mad_u32_u24 v22, v8, s3, v6
	v_or_b32_e32 v6, 4, v1
	v_mul_u32_u24_e32 v6, 0x300, v6
	v_lshlrev_b32_e32 v6, 2, v6
	v_lshl_add_u64 v[8:9], v[2:3], 0, v[6:7]
	v_or_b32_e32 v6, 8, v1
	v_mul_u32_u24_e32 v6, 0x300, v6
	v_lshlrev_b32_e32 v6, 2, v6
	v_lshl_add_u64 v[10:11], v[2:3], 0, v[6:7]
	v_or_b32_e32 v6, 12, v1
	v_mul_u32_u24_e32 v6, 0x300, v6
	v_lshlrev_b32_e32 v6, 2, v6
	v_lshl_add_u64 v[12:13], v[2:3], 0, v[6:7]
	v_or_b32_e32 v6, 16, v1
	v_mul_u32_u24_e32 v6, 0x300, v6
	v_lshlrev_b32_e32 v6, 2, v6
	v_lshl_add_u64 v[14:15], v[2:3], 0, v[6:7]
	v_or_b32_e32 v6, 20, v1
	v_mul_u32_u24_e32 v6, 0x300, v6
	v_lshlrev_b32_e32 v6, 2, v6
	v_lshl_add_u64 v[16:17], v[2:3], 0, v[6:7]
	v_or_b32_e32 v6, 24, v1
	v_mul_u32_u24_e32 v6, 0x300, v6
	v_lshlrev_b32_e32 v6, 2, v6
	v_mul_u32_u24_e32 v4, 0x300, v1
	v_lshl_add_u64 v[18:19], v[2:3], 0, v[6:7]
	v_or_b32_e32 v6, 28, v1
	v_lshlrev_b32_e32 v4, 2, v4
	v_mov_b32_e32 v5, v7
	v_mul_u32_u24_e32 v6, 0x300, v6
	v_lshl_add_u64 v[4:5], v[2:3], 0, v[4:5]
	v_lshlrev_b32_e32 v6, 2, v6
	v_lshl_add_u64 v[20:21], v[2:3], 0, v[6:7]
	global_load_dword v23, v[4:5], off nt
	global_load_dword v24, v[8:9], off nt
	global_load_dword v25, v[10:11], off nt
	global_load_dword v26, v[12:13], off nt
	global_load_dword v27, v[14:15], off nt
	global_load_dword v28, v[16:17], off nt
	global_load_dword v29, v[18:19], off nt
	global_load_dword v30, v[20:21], off nt
	v_or_b32_e32 v4, 32, v1
	v_mul_u32_u24_e32 v4, 0x300, v4
	v_lshlrev_b32_e32 v6, 2, v4
	v_lshl_add_u64 v[4:5], v[2:3], 0, v[6:7]
	v_or_b32_e32 v6, 36, v1
	v_mul_u32_u24_e32 v6, 0x300, v6
	v_lshlrev_b32_e32 v6, 2, v6
	v_lshl_add_u64 v[8:9], v[2:3], 0, v[6:7]
	v_or_b32_e32 v6, 40, v1
	v_mul_u32_u24_e32 v6, 0x300, v6
	v_lshlrev_b32_e32 v6, 2, v6
	v_lshl_add_u64 v[10:11], v[2:3], 0, v[6:7]
	v_or_b32_e32 v6, 44, v1
	v_mul_u32_u24_e32 v6, 0x300, v6
	v_lshlrev_b32_e32 v6, 2, v6
	v_lshl_add_u64 v[12:13], v[2:3], 0, v[6:7]
	v_or_b32_e32 v6, 48, v1
	v_mul_u32_u24_e32 v6, 0x300, v6
	v_lshlrev_b32_e32 v6, 2, v6
	v_lshl_add_u64 v[14:15], v[2:3], 0, v[6:7]
	v_or_b32_e32 v6, 52, v1
	v_mul_u32_u24_e32 v6, 0x300, v6
	v_lshlrev_b32_e32 v6, 2, v6
	v_lshl_add_u64 v[16:17], v[2:3], 0, v[6:7]
	v_or_b32_e32 v6, 56, v1
	v_mul_u32_u24_e32 v6, 0x300, v6
	v_or_b32_e32 v1, 60, v1
	v_lshlrev_b32_e32 v6, 2, v6
	v_mul_u32_u24_e32 v1, 0x300, v1
	v_lshl_add_u64 v[18:19], v[2:3], 0, v[6:7]
	v_lshlrev_b32_e32 v6, 2, v1
	v_lshl_add_u64 v[2:3], v[2:3], 0, v[6:7]
	global_load_dword v1, v[4:5], off nt
	global_load_dword v6, v[8:9], off nt
	global_load_dword v20, v[10:11], off nt
	global_load_dword v21, v[12:13], off nt
	global_load_dword v31, v[14:15], off nt
	global_load_dword v32, v[16:17], off nt
	global_load_dword v33, v[18:19], off nt
	global_load_dword v34, v[2:3], off nt
	v_lshlrev_b32_e32 v2, 3, v0
	v_and_b32_e32 v4, 56, v2
	s_lshl_b32 s1, s1, 7
	s_add_u32 s4, s10, s1
	s_addc_u32 s5, s11, 0
	s_waitcnt vmcnt(15)
	ds_write_b32 v22, v23
	s_waitcnt vmcnt(14)
	ds_write_b32 v22, v24 offset:1040
	s_waitcnt vmcnt(13)
	ds_write_b32 v22, v25 offset:2080
	s_waitcnt vmcnt(12)
	ds_write_b32 v22, v26 offset:3120
	s_waitcnt vmcnt(11)
	ds_write_b32 v22, v27 offset:4160
	s_waitcnt vmcnt(10)
	ds_write_b32 v22, v28 offset:5200
	s_waitcnt vmcnt(9)
	ds_write_b32 v22, v29 offset:6240
	s_waitcnt vmcnt(8)
	ds_write_b32 v22, v30 offset:7280
	s_waitcnt vmcnt(7)
	ds_write_b32 v22, v1 offset:8320
	s_waitcnt vmcnt(6)
	ds_write_b32 v22, v6 offset:9360
	s_waitcnt vmcnt(5)
	ds_write_b32 v22, v20 offset:10400
	s_waitcnt vmcnt(4)
	ds_write_b32 v22, v21 offset:11440
	s_waitcnt vmcnt(3)
	ds_write_b32 v22, v31 offset:12480
	s_waitcnt vmcnt(2)
	ds_write_b32 v22, v32 offset:13520
	s_waitcnt vmcnt(1)
	ds_write_b32 v22, v33 offset:14560
	s_waitcnt vmcnt(0)
	ds_write_b32 v22, v34 offset:15600
	v_lshrrev_b32_e32 v1, 3, v0
	v_lshlrev_b32_e32 v6, 1, v4
	v_mul_u32_u24_e32 v4, 0x104, v4
	v_lshl_add_u32 v4, v1, 2, v4
	v_add_u32_e32 v5, 0x400, v4
	s_waitcnt lgkmcnt(0)
	s_barrier
	ds_read2_b32 v[8:9], v4 offset1:32
	ds_read2_b32 v[10:11], v4 offset0:130 offset1:162
	ds_read2_b32 v[12:13], v5 offset0:4 offset1:36
	ds_read2_b32 v[14:15], v5 offset0:134 offset1:166
	ds_read2_b32 v[16:17], v5 offset0:199 offset1:231
	ds_read2_b32 v[18:19], v5 offset0:69 offset1:101
	ds_read2_b32 v[20:21], v4 offset0:195 offset1:227
	ds_read2_b32 v[22:23], v4 offset0:65 offset1:97
	v_lshl_add_u64 v[2:3], s[4:5], 0, v[6:7]
	s_mov_b64 s[4:5], 0x180000
	v_lshlrev_b32_e32 v1, 11, v1
	v_lshl_add_u64 v[24:25], v[2:3], 0, s[4:5]
	v_lshl_or_b32 v6, s0, 17, v1
	s_waitcnt lgkmcnt(3)
	v_cvt_pk_f16_f32 v5, v14, v16
	s_waitcnt lgkmcnt(2)
	v_cvt_pk_f16_f32 v4, v12, v18
	s_waitcnt lgkmcnt(1)
	v_cvt_pk_f16_f32 v3, v10, v20
	s_waitcnt lgkmcnt(0)
	v_cvt_pk_f16_f32 v2, v8, v22
	v_lshl_add_u64 v[26:27], v[24:25], 0, v[6:7]
	v_or_b32_e32 v6, 0x10000, v6
	global_store_dwordx4 v[26:27], v[2:5], off sc1
	v_lshl_add_u64 v[6:7], v[24:25], 0, v[6:7]
	s_nop 0
	v_cvt_pk_f16_f32 v5, v15, v17
	v_cvt_pk_f16_f32 v4, v13, v19
	v_cvt_pk_f16_f32 v3, v11, v21
	v_cvt_pk_f16_f32 v2, v9, v23
	global_store_dwordx4 v[6:7], v[2:5], off sc1

.LBB0_17:
	s_andn2_b64 vcc, exec, s[0:1]
	s_cbranch_vccnz .LBB0_19
	s_add_i32 s0, s2, 0xfff8
	s_and_b32 s1, s0, 0xff
	s_mulk_i32 s1, 0xab
	s_bfe_u32 s1, s1, 0x5000b
	s_mul_i32 s3, s1, 12
	s_sub_i32 s0, s0, s3
	s_and_b32 s0, s0, 0xff
	s_lshl_b32 s3, s0, 8
	v_and_b32_e32 v1, 63, v0
	v_lshrrev_b32_e32 v8, 6, v0
	s_waitcnt lgkmcnt(0)
	s_add_u32 s4, s14, s3
	s_addc_u32 s5, s15, 0
	v_lshlrev_b32_e32 v6, 2, v1
	v_mov_b32_e32 v7, 0
	v_lshl_or_b32 v1, s1, 6, v8
	s_movk_i32 s3, 0x104
	v_lshl_add_u64 v[2:3], s[4:5], 0, v[6:7]
	v_mad_u32_u24 v22, v8, s3, v6
	v_or_b32_e32 v6, 4, v1
	v_mul_u32_u24_e32 v6, 0x300, v6
	v_lshlrev_b32_e32 v6, 2, v6
	v_lshl_add_u64 v[8:9], v[2:3], 0, v[6:7]
	v_or_b32_e32 v6, 8, v1
	v_mul_u32_u24_e32 v6, 0x300, v6
	v_lshlrev_b32_e32 v6, 2, v6
	v_lshl_add_u64 v[10:11], v[2:3], 0, v[6:7]
	v_or_b32_e32 v6, 12, v1
	v_mul_u32_u24_e32 v6, 0x300, v6
	v_lshlrev_b32_e32 v6, 2, v6
	v_lshl_add_u64 v[12:13], v[2:3], 0, v[6:7]
	v_or_b32_e32 v6, 16, v1
	v_mul_u32_u24_e32 v6, 0x300, v6
	v_lshlrev_b32_e32 v6, 2, v6
	v_lshl_add_u64 v[14:15], v[2:3], 0, v[6:7]
	v_or_b32_e32 v6, 20, v1
	v_mul_u32_u24_e32 v6, 0x300, v6
	v_lshlrev_b32_e32 v6, 2, v6
	v_lshl_add_u64 v[16:17], v[2:3], 0, v[6:7]
	v_or_b32_e32 v6, 24, v1
	v_mul_u32_u24_e32 v6, 0x300, v6
	v_lshlrev_b32_e32 v6, 2, v6
	v_mul_u32_u24_e32 v4, 0x300, v1
	v_lshl_add_u64 v[18:19], v[2:3], 0, v[6:7]
	v_or_b32_e32 v6, 28, v1
	v_lshlrev_b32_e32 v4, 2, v4
	v_mov_b32_e32 v5, v7
	v_mul_u32_u24_e32 v6, 0x300, v6
	v_lshl_add_u64 v[4:5], v[2:3], 0, v[4:5]
	v_lshlrev_b32_e32 v6, 2, v6
	v_lshl_add_u64 v[20:21], v[2:3], 0, v[6:7]
	global_load_dword v23, v[4:5], off nt
	global_load_dword v24, v[8:9], off nt
	global_load_dword v25, v[10:11], off nt
	global_load_dword v26, v[12:13], off nt
	global_load_dword v27, v[14:15], off nt
	global_load_dword v28, v[16:17], off nt
	global_load_dword v29, v[18:19], off nt
	global_load_dword v30, v[20:21], off nt
	v_or_b32_e32 v4, 32, v1
	v_mul_u32_u24_e32 v4, 0x300, v4
	v_lshlrev_b32_e32 v6, 2, v4
	v_lshl_add_u64 v[4:5], v[2:3], 0, v[6:7]
	v_or_b32_e32 v6, 36, v1
	v_mul_u32_u24_e32 v6, 0x300, v6
	v_lshlrev_b32_e32 v6, 2, v6
	v_lshl_add_u64 v[8:9], v[2:3], 0, v[6:7]
	v_or_b32_e32 v6, 40, v1
	v_mul_u32_u24_e32 v6, 0x300, v6
	v_lshlrev_b32_e32 v6, 2, v6
	v_lshl_add_u64 v[10:11], v[2:3], 0, v[6:7]
	v_or_b32_e32 v6, 44, v1
	v_mul_u32_u24_e32 v6, 0x300, v6
	v_lshlrev_b32_e32 v6, 2, v6
	v_lshl_add_u64 v[12:13], v[2:3], 0, v[6:7]
	v_or_b32_e32 v6, 48, v1
	v_mul_u32_u24_e32 v6, 0x300, v6
	v_lshlrev_b32_e32 v6, 2, v6
	v_lshl_add_u64 v[14:15], v[2:3], 0, v[6:7]
	v_or_b32_e32 v6, 52, v1
	v_mul_u32_u24_e32 v6, 0x300, v6
	v_lshlrev_b32_e32 v6, 2, v6
	v_lshl_add_u64 v[16:17], v[2:3], 0, v[6:7]
	v_or_b32_e32 v6, 56, v1
	v_mul_u32_u24_e32 v6, 0x300, v6
	v_or_b32_e32 v1, 60, v1
	v_lshlrev_b32_e32 v6, 2, v6
	v_mul_u32_u24_e32 v1, 0x300, v1
	v_lshl_add_u64 v[18:19], v[2:3], 0, v[6:7]
	v_lshlrev_b32_e32 v6, 2, v1
	v_lshl_add_u64 v[2:3], v[2:3], 0, v[6:7]
	global_load_dword v1, v[4:5], off nt
	global_load_dword v6, v[8:9], off nt
	global_load_dword v20, v[10:11], off nt
	global_load_dword v21, v[12:13], off nt
	global_load_dword v31, v[14:15], off nt
	global_load_dword v32, v[16:17], off nt
	global_load_dword v33, v[18:19], off nt
	global_load_dword v34, v[2:3], off nt
	v_lshlrev_b32_e32 v2, 3, v0
	v_and_b32_e32 v2, 56, v2
	s_lshl_b32 s1, s1, 7
	s_add_u32 s4, s10, s1
	s_addc_u32 s5, s11, 0
	s_waitcnt vmcnt(15)
	ds_write_b32 v22, v23
	s_waitcnt vmcnt(14)
	ds_write_b32 v22, v24 offset:1040
	s_waitcnt vmcnt(13)
	ds_write_b32 v22, v25 offset:2080
	s_waitcnt vmcnt(12)
	ds_write_b32 v22, v26 offset:3120
	s_waitcnt vmcnt(11)
	ds_write_b32 v22, v27 offset:4160
	s_waitcnt vmcnt(10)
	ds_write_b32 v22, v28 offset:5200
	s_waitcnt vmcnt(9)
	ds_write_b32 v22, v29 offset:6240
	s_waitcnt vmcnt(8)
	ds_write_b32 v22, v30 offset:7280
	s_waitcnt vmcnt(7)
	ds_write_b32 v22, v1 offset:8320
	s_waitcnt vmcnt(6)
	ds_write_b32 v22, v6 offset:9360
	s_waitcnt vmcnt(5)
	ds_write_b32 v22, v20 offset:10400
	s_waitcnt vmcnt(4)
	ds_write_b32 v22, v21 offset:11440
	s_waitcnt vmcnt(3)
	ds_write_b32 v22, v31 offset:12480
	s_waitcnt vmcnt(2)
	ds_write_b32 v22, v32 offset:13520
	s_waitcnt vmcnt(1)
	ds_write_b32 v22, v33 offset:14560
	s_waitcnt vmcnt(0)
	ds_write_b32 v22, v34 offset:15600
	v_lshrrev_b32_e32 v1, 3, v0
	v_lshlrev_b32_e32 v6, 1, v2
	v_mul_u32_u24_e32 v2, 0x104, v2
	v_lshl_add_u32 v2, v1, 2, v2
	v_add_u32_e32 v3, 0x400, v2
	s_waitcnt lgkmcnt(0)
	s_barrier
	ds_read2_b32 v[8:9], v2 offset1:32
	ds_read2_b32 v[10:11], v2 offset0:130 offset1:162
	ds_read2_b32 v[12:13], v3 offset0:4 offset1:36
	ds_read2_b32 v[14:15], v3 offset0:134 offset1:166
	ds_read2_b32 v[16:17], v3 offset0:199 offset1:231
	ds_read2_b32 v[18:19], v3 offset0:69 offset1:101
	ds_read2_b32 v[20:21], v2 offset0:195 offset1:227
	ds_read2_b32 v[22:23], v2 offset0:65 offset1:97
	v_lshlrev_b32_e32 v1, 11, v1
	v_lshl_add_u64 v[24:25], s[4:5], 0, v[6:7]
	v_lshl_or_b32 v6, s0, 17, v1
	s_waitcnt lgkmcnt(3)
	v_cvt_pk_f16_f32 v5, v14, v16
	s_waitcnt lgkmcnt(2)
	v_cvt_pk_f16_f32 v4, v12, v18
	s_waitcnt lgkmcnt(1)
	v_cvt_pk_f16_f32 v3, v10, v20
	s_waitcnt lgkmcnt(0)
	v_cvt_pk_f16_f32 v2, v8, v22
	v_lshl_add_u64 v[26:27], v[24:25], 0, v[6:7]
	v_or_b32_e32 v6, 0x10000, v6
	global_store_dwordx4 v[26:27], v[2:5], off sc1
	v_lshl_add_u64 v[6:7], v[24:25], 0, v[6:7]
	s_nop 0
	v_cvt_pk_f16_f32 v5, v15, v17
	v_cvt_pk_f16_f32 v4, v13, v19
	v_cvt_pk_f16_f32 v3, v11, v21
	v_cvt_pk_f16_f32 v2, v9, v23
	global_store_dwordx4 v[6:7], v[2:5], off sc1

.LBB0_20:
	s_andn2_b64 vcc, exec, s[0:1]
	s_cbranch_vccnz .LBB0_22
	v_lshl_or_b32 v1, s2, 8, v0
	v_add_u32_e32 v10, 0xfffff800, v1
	v_mov_b32_e32 v11, 0
	v_lshlrev_b64 v[2:3], 5, v[10:11]
	s_waitcnt lgkmcnt(0)
	v_lshl_add_u64 v[12:13], s[12:13], 0, v[2:3]
	global_load_dwordx4 v[2:5], v[12:13], off nt
	global_load_dwordx4 v[6:9], v[12:13], off offset:16 nt
	v_mov_b32_e32 v12, s8
	v_mov_b32_e32 v13, s9
	s_waitcnt vmcnt(1)
	v_cvt_f16_f32_e32 v1, v2
	v_cvt_pk_f16_f32 v2, v3, v4
	s_waitcnt vmcnt(0)
	v_cvt_pk_f16_f32 v4, v5, v6
	v_cvt_f16_f32_e32 v6, v9
	v_cvt_pk_f16_f32 v5, v7, v8
	v_alignbit_b32 v3, v4, v2, 16
	v_alignbit_b32 v4, v5, v4, 16
	v_pack_b32_f16 v2, v1, v2
	v_alignbit_b32 v5, v6, v5, 16
	v_lshl_add_u64 v[6:7], v[10:11], 4, v[12:13]
	global_store_dwordx4 v[6:7], v[2:5], off sc1
